# v18_wpre
# speedup vs baseline: 1.0423x; 1.0059x over previous
.LBB1_50:
	s_or_b64 exec, exec, s[0:1]
	v_and_b32_e32 v1, 31, v0
	v_lshrrev_b32_e32 v24, 8, v0
	v_mad_u32_u24 v19, v24, 42, v1
	v_min_u32_e32 v20, 0x53, v19
	v_lshrrev_b32_e32 v18, 5, v193
	s_movk_i32 s64, 0x110
	v_mul_u32_u24_e32 v25, 0x110, v20
	v_min_u32_e32 v20, 62, v19
	v_lshlrev_b32_e32 v206, 6, v189
	v_mov_b32_e32 v66, 0
	v_mul_u32_u24_e32 v26, 0x110, v20
	v_lshlrev_b32_e32 v204, 4, v18
	v_mad_u32_u24 v22, v19, s64, v206
	v_lshlrev_b32_e32 v27, 3, v18
	v_lshlrev_b32_e32 v18, 1, v183
	v_mov_b32_e32 v19, v66
	v_lshlrev_b32_e32 v20, 10, v185
	v_lshl_add_u64 v[18:19], s[30:31], 0, v[18:19]
	v_and_b32_e32 v20, 0x1000, v20
	v_mov_b32_e32 v21, v66
	v_lshl_add_u64 v[18:19], v[18:19], 0, v[20:21]
	v_mov_b32_e32 v183, v66
	v_lshl_add_u64 v[18:19], v[18:19], 0, v[182:183]
	s_mov_b64 s[6:7], 0x48000
	v_lshl_add_u64 v[208:209], v[18:19], 0, s[6:7]
	v_lshrrev_b32_e32 v18, 2, v0
	v_and_b32_e32 v29, 8, v18
	v_mul_u32_u24_e32 v18, 0x3000, v189
	v_lshlrev_b32_e32 v210, 2, v193
	v_or_b32_e32 v18, v18, v210
	v_add_u32_e32 v221, 0x15a80, v18
	v_lshlrev_b32_e32 v18, 6, v193
	v_and_b32_e32 v20, 0xe00, v18
	s_add_u32 s34, s18, 0xc000
	s_movk_i32 s3, 0xff
	v_add_u32_e32 v19, 0x25a80, v210
	v_and_b32_e32 v224, 0x800, v18
	v_or_b32_e32 v225, 0x6600, v20
	v_or_b32_e32 v226, 0x7600, v20
	v_or_b32_e32 v227, 0x8600, v20
	v_or_b32_e32 v228, 0x9600, v20
	v_or_b32_e32 v229, 0x600, v20
	v_or_b32_e32 v230, 0x1600, v20
	v_or_b32_e32 v231, 0x2600, v20
	v_or_b32_e32 v232, 0x3600, v20
	v_or_b32_e32 v233, 0x4600, v20
	v_or_b32_e32 v234, 0x5600, v20
	v_lshlrev_b32_e32 v18, 8, v189
	v_lshlrev_b32_e32 v20, 2, v0
	s_addc_u32 s35, s19, 0
	v_cmp_lt_u32_e64 s[6:7], s3, v0
	v_and_b32_e32 v32, 0x7c, v20
	s_lshl_b32 s3, s2, 3
	v_add_u32_e32 v236, v19, v18
	s_lshl_b32 s2, s2, 5
	v_lshlrev_b32_e32 v18, 14, v185
	v_mov_b32_e32 v19, v66
	v_lshlrev_b32_e32 v20, 15, v189
	v_add_u32_e32 v28, 0x10140, v22
	v_add_u32_e32 v30, 0x11790, v22
	s_and_b32 s67, s3, 0x700
	s_and_b32 s2, s2, 0x1f00
	v_lshl_add_u64 v[18:19], s[30:31], 0, v[18:19]
	v_lshl_add_u64 v[20:21], s[30:31], 0, v[20:21]
	v_lshlrev_b32_e32 v22, 14, v24
	v_mov_b32_e32 v23, v66
	s_add_u32 s38, s34, s2
	v_lshl_add_u64 v[18:19], v[18:19], 0, v[182:183]
	s_mov_b64 s[2:3], 0x60000
	v_lshl_add_u64 v[20:21], v[20:21], 0, v[22:23]
	v_or_b32_e32 v220, v212, v1
	v_lshl_add_u64 v[212:213], v[18:19], 0, s[2:3]
	v_lshl_add_u64 v[20:21], v[20:21], 0, v[182:183]
	s_mov_b64 s[2:3], 0xc0000
	v_lshlrev_b32_e32 v33, 7, v185
	v_lshl_add_u64 v[214:215], v[20:21], 0, s[2:3]
	v_or_b32_e32 v23, 64, v1
	s_movk_i32 s69, 0x410
	v_mov_b32_e32 v20, 0x10140
	v_or_b32_e32 v237, v33, v32
	v_and_b32_e32 v18, 0x1c0, v0
	v_or_b32_e32 v22, v27, v33
	v_mad_u32_u24 v33, v23, s69, v20
	v_lshlrev_b32_e32 v20, 2, v32
	v_mov_b32_e32 v21, v66
	v_or_b32_e32 v31, 0x10140, v204
	v_lshlrev_b32_e32 v18, 2, v18
	v_mov_b32_e32 v19, v66
	s_movk_i32 s68, 0x54
	v_lshl_add_u64 v[216:217], s[26:27], 0, v[20:21]
	v_or_b32_e32 v20, 32, v1
	v_min_i32_e32 v21, 0x53, v23
	s_mov_b32 s37, 0
	v_lshl_or_b32 v207, v24, 7, v31
	v_cmp_eq_u32_e64 s[8:9], 1, v24
	v_lshlrev_b32_e32 v222, 2, v220
	v_lshl_add_u64 v[18:19], s[16:17], 0, v[18:19]
	v_cmp_gt_u32_e64 s[12:13], s68, v23
	v_lshl_or_b32 v24, v24, 9, v31
	v_mul_u32_u24_e32 v20, 0x110, v20
	v_mul_u32_u24_e32 v23, 0x110, v21
	v_mul_u32_u24_e32 v31, 0x410, v1
	v_mul_u32_u24_e32 v21, 0x410, v21
	v_mov_b32_e32 v205, v66
	s_mov_b32 s16, 0x18618618
	v_cmp_gt_u32_e64 s[0:1], 32, v193
	v_cmp_lt_u32_e64 s[14:15], 31, v193
	v_cmp_gt_u32_e64 s[4:5], 21, v1
	s_movk_i32 s65, 0x1000
	s_movk_i32 s66, 0x3000
	v_add_u32_e32 v223, 0x25680, v222
	v_lshl_or_b32 v235, v189, 7, v32
	v_cmp_eq_u32_e64 s[10:11], 0, v193
	s_addc_u32 s39, s35, 0
	v_mul_u32_u24_e32 v238, 0x110, v1
	v_add_u32_e32 v239, 0x10140, v22
	s_add_i32 s70, s33, 16
	s_add_i32 s71, s33, 32
	s_add_i32 s72, s33, 48
	s_add_i32 s73, s33, 64
	s_add_i32 s74, s33, 0x50
	v_lshl_add_u64 v[218:219], v[18:19], 0, v[204:205]
	v_add_u32_e32 v205, v25, v184
	v_add_u32_e32 v240, v26, v204
	v_add_u32_e32 v241, v207, v20
	v_add_u32_e32 v242, v207, v23
	s_movk_i32 s75, 0x2000
	s_movk_i32 s76, 0x100
	s_movk_i32 s77, 0xffc0
	s_mov_b32 s17, 0x3f086186
	s_mov_b32 s78, 0xf800000
	v_mov_b32_e32 v243, 0x260
	s_movk_i32 s79, 0x44
	v_add_u32_e32 v244, v33, v22
	v_add_u32_e32 v245, v24, v31
	v_add_u32_e32 v246, v24, v21
	v_add_u32_e32 v247, v28, v27
	v_add_u32_e32 v248, v30, v29
	v_mov_b32_e32 v249, 0x25680
	s_mov_b32 s36, s37
	v_mul_u32_u24_e32 v250, 37, v1
	v_lshrrev_b32_e32 v250, 8, v250
	v_mul_u32_u24_e32 v251, 7, v250
	v_sub_u32_e32 v251, v1, v251
	v_lshlrev_b32_e32 v252, 6, v250
	v_lshl_add_u32 v252, v251, 3, v252
	v_bfe_u32 v251, v0, 5, 1
	v_lshl_add_u32 v252, v251, 2, v252
	v_lshlrev_b32_e32 v250, 6, v1
	v_add_u32_e32 v250, 0xfffff938, v250
	v_cmp_lt_u32_e64 s[84:85], 27, v1
	v_mov_b32_e32 v254, v252
	s_movk_i32 s86, 0x138
	s_nop 1
	v_cndmask_b32_e64 v253, v252, v250, s[84:85]
	v_writelane_b32 v254, s86, 0
	s_nop 0
	v_readfirstlane_b32 s86, v206
	s_lshr_b32 s87, s67, 8
	s_mul_i32 s87, s87, 0x500
	s_mul_i32 s86, s86, 5
	s_add_i32 s86, s86, s87
	s_cmp_eq_u64 s[6:7], 0
	s_cbranch_scc0 .Lprio_skip
	s_setprio 1

.LBB1_53:
	ds_read_b128 v[164:167], v205 offset:43008
	ds_read_b128 v[168:171], v205 offset:43040
	ds_read_b128 v[172:175], v205 offset:43072
	ds_read_b128 v[176:179], v205 offset:43104
	ds_read_b128 v[180:183], v205 offset:43136
	ds_read_b128 v[184:187], v205 offset:43168
	ds_read_b128 v[188:191], v205 offset:43200
	ds_read_b128 v[192:195], v205 offset:43232
	s_waitcnt vmcnt(17) lgkmcnt(7)
	v_mfma_f32_32x32x16_f16 v[34:49], v[112:115], v[164:167], 0
	s_waitcnt vmcnt(0)
	v_mfma_f32_32x32x16_f16 v[18:33], v[116:119], v[164:167], v[2:17]
	s_waitcnt lgkmcnt(6)
	v_mfma_f32_32x32x16_f16 v[34:49], v[100:103], v[168:171], v[34:49]
	v_mfma_f32_32x32x16_f16 v[18:33], v[120:123], v[168:171], v[18:33]
	s_waitcnt lgkmcnt(5)
	v_mfma_f32_32x32x16_f16 v[34:49], v[104:107], v[172:175], v[34:49]
	v_mfma_f32_32x32x16_f16 v[18:33], v[124:127], v[172:175], v[18:33]
	s_waitcnt lgkmcnt(4)
	v_mfma_f32_32x32x16_f16 v[34:49], v[108:111], v[176:179], v[34:49]
	v_mfma_f32_32x32x16_f16 v[18:33], v[128:131], v[176:179], v[18:33]
	s_waitcnt lgkmcnt(3)
	v_mfma_f32_32x32x16_f16 v[34:49], v[132:135], v[180:183], v[34:49]
	v_mfma_f32_32x32x16_f16 v[18:33], v[148:151], v[180:183], v[18:33]
	s_waitcnt lgkmcnt(2)
	v_mfma_f32_32x32x16_f16 v[34:49], v[136:139], v[184:187], v[34:49]
	v_mfma_f32_32x32x16_f16 v[18:33], v[152:155], v[184:187], v[18:33]
	s_waitcnt lgkmcnt(1)
	v_mfma_f32_32x32x16_f16 v[34:49], v[140:143], v[188:191], v[34:49]
	v_mfma_f32_32x32x16_f16 v[18:33], v[156:159], v[188:191], v[18:33]
	s_waitcnt lgkmcnt(0)
	v_mfma_f32_32x32x16_f16 v[34:49], v[144:147], v[192:195], v[34:49]
	v_mfma_f32_32x32x16_f16 v[18:33], v[160:163], v[192:195], v[18:33]
	s_nop 10
	v_cvt_pk_f16_f32 v41, v40, v41
	v_cvt_pk_f16_f32 v40, v38, v39
	v_cvt_pk_f16_f32 v39, v36, v37
	v_cvt_pk_f16_f32 v38, v34, v35
	v_cvt_pk_f16_f32 v25, v24, v25
	v_cvt_pk_f16_f32 v24, v22, v23
	v_cvt_pk_f16_f32 v23, v20, v21
	v_cvt_pk_f16_f32 v22, v18, v19
	v_cvt_pk_f16_f32 v21, v48, v49
	v_cvt_pk_f16_f32 v20, v46, v47
	v_cvt_pk_f16_f32 v19, v44, v45
	v_cvt_pk_f16_f32 v18, v42, v43
	v_mfma_f32_32x32x16_f16 v[50:65], v[38:41], v[22:25], 0
	v_cvt_pk_f16_f32 v25, v32, v33
	v_cvt_pk_f16_f32 v24, v30, v31
	v_cvt_pk_f16_f32 v23, v28, v29
	v_cvt_pk_f16_f32 v22, v26, v27
	s_nop 1
	v_mfma_f32_32x32x16_f16 v[34:49], v[18:21], v[22:25], 0
	v_mfma_f32_32x32x16_f16 v[18:33], v[164:167], v[96:99], 0
	v_mfma_f32_32x32x16_f16 v[18:33], v[168:171], v[76:79], v[18:33]
	s_nop 2
	v_max3_f32 v250, v50, v51, v52
	v_max3_f32 v250, v250, v53, v54
	v_max3_f32 v250, v250, v55, v56
	v_max3_f32 v250, v250, v57, v58
	v_max_f32_e32 v251, v60, v61
	v_mfma_f32_32x32x16_f16 v[18:33], v[172:175], v[72:75], v[18:33]
	v_max3_f32 v251, v250, v59, v251
	v_cndmask_b32_e64 v250, v250, v251, s[0:1]
	v_mov_b32_e32 v251, v250
	s_nop 1
	v_permlane32_swap_b32_e32 v250, v251
	v_max_f32_e32 v46, v250, v251
	v_mfma_f32_32x32x16_f16 v[18:33], v[176:179], v[68:71], v[18:33]
	v_sub_f32_e32 v47, v50, v46
	v_exp_f32_e32 v50, v47
	v_sub_f32_e32 v47, v51, v46
	v_sub_f32_e32 v48, v52, v46
	v_exp_f32_e32 v51, v47
	v_exp_f32_e32 v52, v48
	v_sub_f32_e32 v48, v53, v46
	v_sub_f32_e32 v49, v55, v46
	v_mfma_f32_32x32x16_f16 v[18:33], v[180:183], v[92:95], v[18:33]
	v_sub_f32_e32 v53, v57, v46
	v_exp_f32_e32 v55, v49
	v_sub_f32_e32 v49, v56, v46
	v_exp_f32_e32 v56, v53
	v_sub_f32_e32 v53, v58, v46
	v_exp_f32_e32 v62, v48
	v_sub_f32_e32 v48, v54, v46
	v_exp_f32_e32 v57, v53
	v_mfma_f32_32x32x16_f16 v[18:33], v[184:187], v[84:87], v[18:33]
	v_sub_f32_e32 v53, v59, v46
	v_exp_f32_e32 v48, v48
	v_exp_f32_e32 v53, v53
	v_add_f32_e32 v47, v51, v50
	v_add_f32_e32 v47, v52, v47
	v_exp_f32_e32 v49, v49
	v_add_f32_e32 v47, v62, v47
	v_mfma_f32_32x32x16_f16 v[18:33], v[188:191], v[88:91], v[18:33]
	v_add_f32_e32 v47, v48, v47
	v_cndmask_b32_e64 v58, v53, 0, s[14:15]
	v_sub_f32_e32 v53, v60, v46
	v_sub_f32_e32 v46, v61, v46
	v_add_f32_e32 v47, v55, v47
	v_exp_f32_e32 v53, v53
	v_exp_f32_e32 v46, v46
	v_add_f32_e32 v47, v49, v47
	v_mfma_f32_32x32x16_f16 v[18:33], v[192:195], v[80:83], v[18:33]
	ds_read_b128 v[192:195], v240 offset:48720
	ds_read_b128 v[188:191], v240 offset:48752
	ds_read_b128 v[184:187], v240 offset:48784
	ds_read_b128 v[180:183], v240 offset:48816
	ds_read_b128 v[176:179], v240 offset:48848
	ds_read_b128 v[172:175], v240 offset:48880
	ds_read_b128 v[168:171], v240 offset:48912
	ds_read_b128 v[164:167], v240 offset:48944
	v_add_f32_e32 v47, v56, v47
	v_add_f32_e32 v47, v57, v47
	v_add_f32_e32 v47, v58, v47
	v_cndmask_b32_e64 v59, v53, 0, s[14:15]
	v_cndmask_b32_e64 v60, v46, 0, s[14:15]
	v_cvt_pk_f16_f32 v46, v50, v51
	v_max3_f32 v50, v34, v35, v36
	v_add_f32_e32 v47, v59, v47
	v_max3_f32 v50, v50, v37, v38
	v_add_f32_e32 v53, v60, v47
	v_cvt_pk_f16_f32 v47, v52, v62
	v_max3_f32 v50, v50, v39, v40
	v_max3_f32 v50, v50, v41, v42
	v_max_f32_e32 v51, v44, v45
	v_max3_f32 v51, v50, v43, v51
	v_cndmask_b32_e64 v50, v50, v51, s[0:1]
	v_mov_b32_e32 v51, v50
	s_nop 1
	v_permlane32_swap_b32_e32 v50, v51
	s_waitcnt lgkmcnt(7)
	v_mfma_f32_32x32x16_f16 v[2:17], v[116:119], v[192:195], v[2:17]
	v_max_f32_e32 v50, v50, v51
	v_sub_f32_e32 v34, v34, v50
	v_exp_f32_e32 v52, v34
	v_sub_f32_e32 v34, v35, v50
	v_sub_f32_e32 v35, v36, v50
	s_waitcnt lgkmcnt(6)
	v_mfma_f32_32x32x16_f16 v[2:17], v[120:123], v[188:191], v[2:17]
	v_cvt_pk_f16_f32 v49, v49, v56
	v_exp_f32_e32 v56, v35
	v_sub_f32_e32 v35, v37, v50
	v_cvt_pk_f16_f32 v64, v57, v58
	v_exp_f32_e32 v57, v35
	v_sub_f32_e32 v35, v38, v50
	v_exp_f32_e32 v58, v35
	s_waitcnt lgkmcnt(5)
	v_mfma_f32_32x32x16_f16 v[2:17], v[124:127], v[184:187], v[2:17]
	v_sub_f32_e32 v35, v39, v50
	v_cvt_pk_f16_f32 v65, v59, v60
	v_exp_f32_e32 v60, v35
	v_sub_f32_e32 v35, v40, v50
	v_cvt_pk_f16_f32 v48, v48, v55
	v_exp_f32_e32 v55, v34
	v_exp_f32_e32 v62, v35
	s_waitcnt lgkmcnt(4)
	v_mfma_f32_32x32x16_f16 v[2:17], v[128:131], v[180:183], v[2:17]
	v_sub_f32_e32 v35, v41, v50
	v_exp_f32_e32 v63, v35
	v_sub_f32_e32 v35, v42, v50
	v_exp_f32_e32 v59, v35
	v_sub_f32_e32 v35, v43, v50
	v_exp_f32_e32 v35, v35
	s_waitcnt lgkmcnt(3)
	v_mfma_f32_32x32x16_f16 v[2:17], v[148:151], v[176:179], v[2:17]
	v_add_f32_e32 v34, v55, v52
	v_add_f32_e32 v34, v56, v34
	v_add_f32_e32 v34, v57, v34
	v_add_f32_e32 v34, v58, v34
	v_cndmask_b32_e64 v61, v35, 0, s[14:15]
	v_sub_f32_e32 v35, v44, v50
	v_add_f32_e32 v34, v60, v34
	s_waitcnt lgkmcnt(2)
	v_mfma_f32_32x32x16_f16 v[2:17], v[152:155], v[172:175], v[2:17]
	v_exp_f32_e32 v35, v35
	v_sub_f32_e32 v36, v45, v50
	v_cvt_pk_f16_f32 v25, v24, v25
	v_cvt_pk_f16_f32 v24, v22, v23
	v_cvt_pk_f16_f32 v23, v20, v21
	v_cvt_pk_f16_f32 v22, v18, v19
	v_add_f32_e32 v34, v62, v34
	s_waitcnt lgkmcnt(1)
	v_mfma_f32_32x32x16_f16 v[2:17], v[156:159], v[168:171], v[2:17]
	v_exp_f32_e32 v36, v36
	v_add_f32_e32 v34, v63, v34
	v_add_f32_e32 v34, v59, v34
	v_add_f32_e32 v34, v61, v34
	v_cndmask_b32_e64 v211, v35, 0, s[14:15]
	v_add_f32_e32 v18, v211, v34
	s_waitcnt lgkmcnt(0)
	v_mfma_f32_32x32x16_f16 v[2:17], v[160:163], v[164:167], v[2:17]
	v_cndmask_b32_e64 v250, v36, 0, s[14:15]
	v_cvt_pk_f16_f32 v51, v32, v33
	v_mfma_f32_32x32x16_f16 v[32:47], v[22:25], v[46:49], 0
	v_cvt_pk_f16_f32 v50, v30, v31
	v_cvt_pk_f16_f32 v49, v28, v29
	v_cvt_pk_f16_f32 v48, v26, v27
	v_mov_b32_e32 v67, v66
	v_add_f32_e32 v251, v250, v18
	v_mov_b32_e32 v54, v53
	v_mov_b32_e32 v252, v251
	v_mfma_f32_32x32x16_f16 v[32:47], v[48:51], v[64:67], v[32:47]
	v_permlane32_swap_b32_e32 v53, v54
	v_permlane32_swap_b32_e32 v251, v252
	s_and_saveexec_b64 s[2:3], s[4:5]
	s_cbranch_execz .LBB1_55
	v_add_f32_e32 v18, v53, v54
	v_rcp_f32_e32 v18, v18
	s_nop 5
	v_pk_mul_f32 v[32:33], v[32:33], v[18:19] op_sel_hi:[1,0]
	v_pk_mul_f32 v[34:35], v[34:35], v[18:19] op_sel_hi:[1,0]
	v_pk_mul_f32 v[36:37], v[36:37], v[18:19] op_sel_hi:[1,0]
	v_pk_mul_f32 v[38:39], v[38:39], v[18:19] op_sel_hi:[1,0]
	v_cvt_pk_f16_f32 v20, v32, v33
	v_cvt_pk_f16_f32 v21, v34, v35
	v_cvt_pk_f16_f32 v26, v36, v37
	v_cvt_pk_f16_f32 v27, v38, v39
	ds_write2_b64 v247, v[20:21], v[26:27] offset1:2

.LBB1_57:
	s_or_b64 exec, exec, s[2:3]
	s_waitcnt lgkmcnt(7)
	v_mfma_f32_32x32x16_f16 v[18:33], v[112:115], v[192:195], 0
	s_lshl_b64 s[2:3], s[36:37], 15
	v_lshl_add_u64 v[34:35], v[208:209], 0, s[2:3]
	s_waitcnt lgkmcnt(6)
	v_mfma_f32_32x32x16_f16 v[18:33], v[100:103], v[188:191], v[18:33]
	global_load_dwordx4 v[100:103], v[34:35], off
	global_load_dwordx4 v[58:61], v[34:35], off offset:1024
	global_load_dwordx4 v[54:57], v[34:35], off offset:2048
	global_load_dwordx4 v[50:53], v[34:35], off offset:3072
	s_waitcnt lgkmcnt(5)
	v_mfma_f32_32x32x16_f16 v[18:33], v[104:107], v[184:187], v[18:33]
	s_waitcnt lgkmcnt(4)
	v_mfma_f32_32x32x16_f16 v[18:33], v[108:111], v[180:183], v[18:33]
	s_waitcnt lgkmcnt(3)
	v_mfma_f32_32x32x16_f16 v[18:33], v[132:135], v[176:179], v[18:33]
	s_waitcnt lgkmcnt(2)
	v_mfma_f32_32x32x16_f16 v[18:33], v[136:139], v[172:175], v[18:33]
	s_waitcnt lgkmcnt(1)
	v_mfma_f32_32x32x16_f16 v[18:33], v[140:143], v[168:171], v[18:33]
	s_waitcnt lgkmcnt(0)
	v_mfma_f32_32x32x16_f16 v[18:33], v[144:147], v[164:167], v[18:33]
	s_nop 11
	v_cvt_pk_f16_f32 v25, v24, v25
	v_cvt_pk_f16_f32 v24, v22, v23
	v_cvt_pk_f16_f32 v23, v20, v21
	v_cvt_pk_f16_f32 v22, v18, v19
	v_cvt_pk_f16_f32 v9, v8, v9
	v_cvt_pk_f16_f32 v8, v6, v7
	v_cvt_pk_f16_f32 v7, v4, v5
	v_cvt_pk_f16_f32 v6, v2, v3
	v_cvt_pk_f16_f32 v5, v32, v33
	v_cvt_pk_f16_f32 v4, v30, v31
	v_mfma_f32_32x32x16_f16 v[34:49], v[22:25], v[6:9], 0
	v_cvt_pk_f16_f32 v3, v28, v29
	v_cvt_pk_f16_f32 v2, v26, v27
	v_cvt_pk_f16_f32 v9, v16, v17
	v_cvt_pk_f16_f32 v8, v14, v15
	v_cvt_pk_f16_f32 v7, v12, v13
	v_cvt_pk_f16_f32 v6, v10, v11
	v_mov_b32_e32 v67, v66
	s_nop 0
	v_mfma_f32_32x32x16_f16 v[18:33], v[2:5], v[6:9], 0
	s_nop 2
	v_max3_f32 v2, v34, v35, v36
	v_max3_f32 v2, v2, v37, v38
	s_nop 6
	v_max3_f32 v30, v2, v39, v40
	v_mfma_f32_32x32x16_f16 v[2:17], v[192:195], v[96:99], 0
	v_max3_f32 v30, v30, v41, v42
	v_max_f32_e32 v31, v44, v45
	v_max3_f32 v31, v30, v43, v31
	v_cndmask_b32_e64 v30, v30, v31, s[0:1]
	v_mov_b32_e32 v31, v30
	v_mfma_f32_32x32x16_f16 v[2:17], v[188:191], v[76:79], v[2:17]
	s_nop 0
	v_permlane32_swap_b32_e32 v30, v31
	v_max_f32_e32 v30, v30, v31
	v_sub_f32_e32 v31, v34, v30
	v_exp_f32_e32 v34, v31
	v_mfma_f32_32x32x16_f16 v[2:17], v[184:187], v[72:75], v[2:17]
	v_sub_f32_e32 v31, v35, v30
	v_sub_f32_e32 v33, v37, v30
	v_exp_f32_e32 v35, v31
	v_sub_f32_e32 v31, v36, v30
	v_exp_f32_e32 v36, v33
	v_sub_f32_e32 v33, v38, v30
	v_exp_f32_e32 v46, v33
	v_mfma_f32_32x32x16_f16 v[2:17], v[180:183], v[68:71], v[2:17]
	v_sub_f32_e32 v33, v39, v30
	v_sub_f32_e32 v37, v41, v30
	v_exp_f32_e32 v39, v33
	v_sub_f32_e32 v33, v40, v30
	v_exp_f32_e32 v40, v37
	v_sub_f32_e32 v37, v42, v30
	v_exp_f32_e32 v41, v37
	v_sub_f32_e32 v37, v43, v30
	v_exp_f32_e32 v37, v37
	v_mfma_f32_32x32x16_f16 v[2:17], v[176:179], v[92:95], v[2:17]
	v_exp_f32_e32 v31, v31
	v_cndmask_b32_e64 v42, v37, 0, s[14:15]
	v_sub_f32_e32 v37, v44, v30
	v_sub_f32_e32 v30, v45, v30
	v_exp_f32_e32 v30, v30
	v_add_f32_e32 v32, v35, v34
	v_mfma_f32_32x32x16_f16 v[2:17], v[172:175], v[84:87], v[2:17]
	v_add_f32_e32 v32, v31, v32
	v_cndmask_b32_e64 v44, v30, 0, s[14:15]
	v_cvt_pk_f16_f32 v30, v34, v35
	v_max3_f32 v34, v18, v19, v20
	v_max3_f32 v34, v34, v21, v22
	v_add_f32_e32 v32, v36, v32
	v_cvt_pk_f16_f32 v31, v31, v36
	v_max3_f32 v34, v34, v23, v24
	v_max3_f32 v34, v34, v25, v26
	v_max_f32_e32 v35, v28, v29
	v_max3_f32 v35, v34, v27, v35
	v_cndmask_b32_e64 v34, v34, v35, s[0:1]
	v_exp_f32_e32 v33, v33
	v_mov_b32_e32 v35, v34
	s_nop 1
	v_permlane32_swap_b32_e32 v34, v35
	v_add_f32_e32 v32, v46, v32
	v_mfma_f32_32x32x16_f16 v[2:17], v[168:171], v[88:91], v[2:17]
	v_add_f32_e32 v32, v39, v32
	v_exp_f32_e32 v37, v37
	v_max_f32_e32 v34, v34, v35
	v_add_f32_e32 v32, v33, v32
	v_sub_f32_e32 v18, v18, v34
	v_add_f32_e32 v32, v40, v32
	v_exp_f32_e32 v36, v18
	v_sub_f32_e32 v18, v19, v34
	v_sub_f32_e32 v19, v20, v34
	v_add_f32_e32 v32, v41, v32
	v_cvt_pk_f16_f32 v33, v33, v40
	v_exp_f32_e32 v40, v19
	v_sub_f32_e32 v19, v21, v34
	v_add_f32_e32 v32, v42, v32
	v_cndmask_b32_e64 v43, v37, 0, s[14:15]
	v_cvt_pk_f16_f32 v64, v41, v42
	v_exp_f32_e32 v41, v19
	v_sub_f32_e32 v19, v22, v34
	v_add_f32_e32 v32, v43, v32
	v_exp_f32_e32 v42, v19
	v_sub_f32_e32 v19, v23, v34
	v_add_f32_e32 v37, v44, v32
	v_cvt_pk_f16_f32 v65, v43, v44
	v_exp_f32_e32 v44, v19
	v_sub_f32_e32 v19, v24, v34
	v_mfma_f32_32x32x16_f16 v[2:17], v[164:167], v[80:83], v[2:17]
	v_cvt_pk_f16_f32 v32, v46, v39
	v_exp_f32_e32 v39, v18
	v_exp_f32_e32 v46, v19
	v_sub_f32_e32 v19, v25, v34
	v_exp_f32_e32 v47, v19
	v_sub_f32_e32 v19, v26, v34
	v_exp_f32_e32 v43, v19
	v_sub_f32_e32 v19, v27, v34
	v_exp_f32_e32 v19, v19
	v_add_f32_e32 v18, v39, v36
	v_add_f32_e32 v18, v40, v18
	v_add_f32_e32 v18, v41, v18
	v_add_f32_e32 v18, v42, v18
	v_cndmask_b32_e64 v45, v19, 0, s[14:15]
	v_sub_f32_e32 v19, v28, v34
	v_add_f32_e32 v18, v44, v18
	v_exp_f32_e32 v19, v19
	v_sub_f32_e32 v20, v29, v34
	v_cvt_pk_f16_f32 v9, v8, v9
	v_cvt_pk_f16_f32 v8, v6, v7
	v_cvt_pk_f16_f32 v7, v4, v5
	v_cvt_pk_f16_f32 v6, v2, v3
	v_add_f32_e32 v18, v46, v18
	v_exp_f32_e32 v20, v20
	v_add_f32_e32 v18, v47, v18
	v_add_f32_e32 v18, v43, v18
	v_add_f32_e32 v18, v45, v18
	v_cndmask_b32_e64 v48, v19, 0, s[14:15]
	v_add_f32_e32 v2, v48, v18
	v_cndmask_b32_e64 v49, v20, 0, s[14:15]
	v_cvt_pk_f16_f32 v35, v16, v17
	v_mfma_f32_32x32x16_f16 v[16:31], v[6:9], v[30:33], 0
	v_cvt_pk_f16_f32 v34, v14, v15
	v_cvt_pk_f16_f32 v33, v12, v13
	v_cvt_pk_f16_f32 v32, v10, v11
	v_add_f32_e32 v62, v49, v2
	v_mov_b32_e32 v38, v37
	v_mov_b32_e32 v63, v62
	s_nop 0
	v_permlane32_swap_b32_e32 v37, v38
	v_mfma_f32_32x32x16_f16 v[16:31], v[32:35], v[64:67], v[16:31]
	v_permlane32_swap_b32_e32 v62, v63
	s_and_saveexec_b64 s[2:3], s[4:5]
	s_cbranch_execz .LBB1_59
	v_add_f32_e32 v2, v37, v38
	v_rcp_f32_e32 v2, v2
	s_nop 6
	v_pk_mul_f32 v[16:17], v[16:17], v[2:3] op_sel_hi:[1,0]
	v_pk_mul_f32 v[18:19], v[18:19], v[2:3] op_sel_hi:[1,0]
	v_pk_mul_f32 v[20:21], v[20:21], v[2:3] op_sel_hi:[1,0]
	v_pk_mul_f32 v[22:23], v[22:23], v[2:3] op_sel_hi:[1,0]
	v_cvt_pk_f16_f32 v4, v16, v17
	v_cvt_pk_f16_f32 v5, v18, v19
	v_cvt_pk_f16_f32 v10, v20, v21
	v_cvt_pk_f16_f32 v11, v22, v23
	ds_write2_b64 v248, v[4:5], v[10:11] offset1:2

.Lep1_join:
	s_waitcnt lgkmcnt(0)
	s_barrier
	s_cmp_eq_u64 s[6:7], 0
	s_cbranch_scc0 .Lep1_w1
	ds_read_b32 v50, v236
	s_mul_i32 s43, s36, 0x5000
	s_add_i32 s43, s43, s86
	s_add_u32 s40, s18, s43
	s_addc_u32 s41, s19, 0
	s_waitcnt lgkmcnt(0)
	v_add_f32_e32 v22, v22, v50
	v_mov_b32_e32 v59, v22
	v_cndmask_b32_e64 v57, v22, 1.0, s[84:85]
	v_writelane_b32 v59, 1.0, 0
	s_mov_b64 s[44:45], exec
	s_mov_b32 exec_lo, -1
	s_mov_b32 exec_hi, 0xfffffff
	global_atomic_add_f32 v253, v57, s[40:41]
	s_mov_b32 exec_lo, 0xf0000001
	s_mov_b32 exec_hi, 0xf0000000
	global_atomic_add_f32 v254, v59, s[40:41]
	s_mov_b64 exec, s[44:45]
	ds_write2st64_b32 v67, v34, v35 offset0:0 offset1:2
	ds_write2st64_b32 v67, v36, v37 offset0:4 offset1:6
	ds_write2st64_b32 v67, v38, v39 offset0:16 offset1:18
	ds_write2st64_b32 v67, v40, v41 offset0:20 offset1:22
	ds_write2st64_b32 v67, v42, v43 offset0:32 offset1:34
	ds_write2st64_b32 v67, v44, v45 offset0:36 offset1:38
	ds_write2st64_b32 v67, v46, v47 offset0:48 offset1:50
	ds_write2st64_b32 v67, v48, v49 offset0:52 offset1:54
	ds_write2st64_b32 v67, v2, v3 offset0:64 offset1:66
	ds_write2st64_b32 v67, v4, v5 offset0:68 offset1:70
	ds_write2st64_b32 v67, v6, v7 offset0:80 offset1:82
	ds_write2st64_b32 v67, v8, v9 offset0:84 offset1:86
	s_branch .Lep1_end

.Lep2_join:
	s_waitcnt lgkmcnt(0)
	s_barrier
	s_cmp_eq_u64 s[6:7], 0
	s_cbranch_scc0 .Lep2_w1
	ds_read_b32 v50, v236
	s_mul_i32 s43, s36, 0x5000
	s_addk_i32 s43, 0x2800
	s_add_i32 s43, s43, s86
	s_add_u32 s40, s18, s43
	s_addc_u32 s41, s19, 0
	s_waitcnt lgkmcnt(0)
	v_add_f32_e32 v22, v22, v50
	v_mov_b32_e32 v59, v22
	v_cndmask_b32_e64 v57, v22, 1.0, s[84:85]
	v_writelane_b32 v59, 1.0, 0
	s_mov_b64 s[44:45], exec
	s_mov_b32 exec_lo, -1
	s_mov_b32 exec_hi, 0xfffffff
	global_atomic_add_f32 v253, v57, s[40:41]
	s_mov_b32 exec_lo, 0xf0000001
	s_mov_b32 exec_hi, 0xf0000000
	global_atomic_add_f32 v254, v59, s[40:41]
	s_mov_b64 exec, s[44:45]
	ds_write2st64_b32 v67, v34, v35 offset0:0 offset1:2
	ds_write2st64_b32 v67, v36, v37 offset0:4 offset1:6
	ds_write2st64_b32 v67, v38, v39 offset0:16 offset1:18
	ds_write2st64_b32 v67, v40, v41 offset0:20 offset1:22
	ds_write2st64_b32 v67, v42, v43 offset0:32 offset1:34
	ds_write2st64_b32 v67, v44, v45 offset0:36 offset1:38
	ds_write2st64_b32 v67, v46, v47 offset0:48 offset1:50
	ds_write2st64_b32 v67, v48, v49 offset0:52 offset1:54
	ds_write2st64_b32 v67, v2, v3 offset0:64 offset1:66
	ds_write2st64_b32 v67, v4, v5 offset0:68 offset1:70
	ds_write2st64_b32 v67, v6, v7 offset0:80 offset1:82
	ds_write2st64_b32 v67, v8, v9 offset0:84 offset1:86
	s_branch .Lep2_end

	.amdhsa_kernel _Z6k_main8MainArgs
		.amdhsa_group_segment_fixed_size 155264
		.amdhsa_private_segment_fixed_size 0
		.amdhsa_kernarg_size 120
		.amdhsa_user_sgpr_count 2
		.amdhsa_user_sgpr_dispatch_ptr 0
		.amdhsa_user_sgpr_queue_ptr 0
		.amdhsa_user_sgpr_kernarg_segment_ptr 1
		.amdhsa_user_sgpr_dispatch_id 0
		.amdhsa_user_sgpr_kernarg_preload_length 0
		.amdhsa_user_sgpr_kernarg_preload_offset 0
		.amdhsa_user_sgpr_private_segment_size 0
		.amdhsa_uses_dynamic_stack 0
		.amdhsa_enable_private_segment 0
		.amdhsa_system_sgpr_workgroup_id_x 1
		.amdhsa_system_sgpr_workgroup_id_y 0
		.amdhsa_system_sgpr_workgroup_id_z 0
		.amdhsa_system_sgpr_workgroup_info 0
		.amdhsa_system_vgpr_workitem_id 0
		.amdhsa_next_free_vgpr 256
		.amdhsa_next_free_sgpr 96
		.amdhsa_accum_offset 256
		.amdhsa_reserve_vcc 1
		.amdhsa_float_round_mode_32 0
		.amdhsa_float_round_mode_16_64 0
		.amdhsa_float_denorm_mode_32 3
		.amdhsa_float_denorm_mode_16_64 3
		.amdhsa_dx10_clamp 1
		.amdhsa_ieee_mode 1
		.amdhsa_fp16_overflow 0
		.amdhsa_tg_split 0
		.amdhsa_exception_fp_ieee_invalid_op 0
		.amdhsa_exception_fp_denorm_src 0
		.amdhsa_exception_fp_ieee_div_zero 0
		.amdhsa_exception_fp_ieee_overflow 0
		.amdhsa_exception_fp_ieee_underflow 0
		.amdhsa_exception_fp_ieee_inexact 0
		.amdhsa_exception_int_div_zero 0
	.end_amdhsa_kernel

amdhsa.kernels:
  - .agpr_count:     0
    .args:
      - .actual_access:  read_only
        .address_space:  global
        .offset:         0
        .size:           8
        .value_kind:     global_buffer
      - .actual_access:  read_only
        .address_space:  global
        .offset:         8
        .size:           8
        .value_kind:     global_buffer
      - .actual_access:  read_only
        .address_space:  global
        .offset:         16
        .size:           8
        .value_kind:     global_buffer
      - .actual_access:  read_only
        .address_space:  global
        .offset:         24
        .size:           8
        .value_kind:     global_buffer
      - .actual_access:  read_only
        .address_space:  global
        .offset:         32
        .size:           8
        .value_kind:     global_buffer
      - .actual_access:  read_only
        .address_space:  global
        .offset:         40
        .size:           8
        .value_kind:     global_buffer
      - .actual_access:  read_only
        .address_space:  global
        .offset:         48
        .size:           8
        .value_kind:     global_buffer
      - .actual_access:  read_only
        .address_space:  global
        .offset:         56
        .size:           8
        .value_kind:     global_buffer
      - .actual_access:  read_only
        .address_space:  global
        .offset:         64
        .size:           8
        .value_kind:     global_buffer
      - .actual_access:  read_only
        .address_space:  global
        .offset:         72
        .size:           8
        .value_kind:     global_buffer
      - .actual_access:  read_only
        .address_space:  global
        .offset:         80
        .size:           8
        .value_kind:     global_buffer
      - .actual_access:  write_only
        .address_space:  global
        .offset:         88
        .size:           8
        .value_kind:     global_buffer
      - .actual_access:  write_only
        .address_space:  global
        .offset:         96
        .size:           8
        .value_kind:     global_buffer
      - .actual_access:  write_only
        .address_space:  global
        .offset:         104
        .size:           8
        .value_kind:     global_buffer
      - .actual_access:  read_only
        .address_space:  global
        .offset:         112
        .size:           8
        .value_kind:     global_buffer
      - .actual_access:  read_only
        .address_space:  global
        .offset:         120
        .size:           8
        .value_kind:     global_buffer
      - .actual_access:  read_only
        .address_space:  global
        .offset:         128
        .size:           8
        .value_kind:     global_buffer
      - .actual_access:  read_only
        .address_space:  global
        .offset:         136
        .size:           8
        .value_kind:     global_buffer
      - .actual_access:  read_only
        .address_space:  global
        .offset:         144
        .size:           8
        .value_kind:     global_buffer
      - .actual_access:  read_only
        .address_space:  global
        .offset:         152
        .size:           8
        .value_kind:     global_buffer
      - .actual_access:  read_only
        .address_space:  global
        .offset:         160
        .size:           8
        .value_kind:     global_buffer
      - .actual_access:  read_only
        .address_space:  global
        .offset:         168
        .size:           8
        .value_kind:     global_buffer
      - .actual_access:  read_only
        .address_space:  global
        .offset:         176
        .size:           8
        .value_kind:     global_buffer
    .group_segment_fixed_size: 1024
    .kernarg_segment_align: 8
    .kernarg_segment_size: 184
    .language:       OpenCL C
    .language_version:
      - 2
      - 0
    .max_flat_workgroup_size: 256
    .name:           _Z6k_prepPKfS0_S0_S0_S0_S0_S0_S0_S0_S0_S0_PfPDF16_S1_S0_S0_S0_S0_S0_S0_S0_S0_S0_
    .private_segment_fixed_size: 0
    .sgpr_count:     28
    .sgpr_spill_count: 0
    .symbol:         _Z6k_prepPKfS0_S0_S0_S0_S0_S0_S0_S0_S0_S0_PfPDF16_S1_S0_S0_S0_S0_S0_S0_S0_S0_S0_.kd
    .uniform_work_group_size: 1
    .uses_dynamic_stack: false
    .vgpr_count:     53
    .vgpr_spill_count: 0
    .wavefront_size: 64
  - .agpr_count:     0
    .args:
      - .offset:         0
        .size:           120
        .value_kind:     by_value
    .group_segment_fixed_size: 155264
    .kernarg_segment_align: 8
    .kernarg_segment_size: 120
    .language:       OpenCL C
    .language_version:
      - 2
      - 0
    .max_flat_workgroup_size: 512
    .name:           _Z6k_main8MainArgs
    .private_segment_fixed_size: 0
    .sgpr_count:     89
    .sgpr_spill_count: 0
    .symbol:         _Z6k_main8MainArgs.kd
    .uniform_work_group_size: 1
    .uses_dynamic_stack: false
    .vgpr_count:     256
    .vgpr_spill_count: 0
    .wavefront_size: 64
